# down-projection GEMM: weight-tile rows re-permuted so each lane owns 16 contiguous output bytes; one 16-byte store per row block instead of two 8-byte stores (half the write requests)
# speedup vs baseline: 1.0165x; 1.0068x over previous
; #define PG8_STAGE(bufoff, gbase, voff) do { _Pragma("unroll") for (int _i = 0; _i < 2; ++_i) \
;         __builtin_amdgcn_raw_ptr_buffer_load_lds(rsrc, (LAS void*)(lds + (bufoff) + ldsw + _i * 8192), 16, (int)(voff)[_i], (int)(gbase), 0, 0); } while (0)
; #define PG8_STAGE_A(bufoff, h, goff) do { if constexpr (GATHER) { PG8_STAGE(bufoff, goff, vG[h]); } else { PG8_STAGE(bufoff, (goff) + (h) * hstep, voffA); } } while (0)
; #define PG8_WAIT_V(n) asm volatile("s_waitcnt vmcnt(" #n ")" ::: "memory")
; #define PG8_BAR __builtin_amdgcn_s_barrier()
;     ...
;     for (int i = 0; i < 2; ++i) { int R, C;
;         { const int b = tid * 16 + i * 8192; const int p = (b >> 7) & 15, fr_ = ((p & 1) << 3) | (p >> 1); R = (b >> 11) * 16 + fr_; C = ((((b >> 4) & 7) ^ (fr_ & 7))) * 16; }
;         const int Rb = Epi::PERM ? ((R & ~31) + perm32(R & 31)) : R;
;         voffA[i] = (unsigned)(R * KB + C); voffB[i] = (unsigned)(Rb * KB + C); }
;     ...
;     if constexpr (SP2) {
;         PG8_STAGE(PG8_SB(0, 0), cB, voffB); PG8_STAGE(PG8_SB(0, 1), cB + hstep, voffB); PG8_STAGE_A(PG8_SA(0, 0), 0, cA); PG8_STAGE_A(PG8_SA(0, 1), 1, cA);
;         if (wr == 1) PG8_BAR;
;         PG8_WAIT_V(2); PG8_BAR;
;         PG8_STAGE(PG8_SB(1, 0), cB + kstep, voffB); PG8_STAGE_A(PG8_SA(1, 0), 0, cA + kstep); PG8_STAGE(PG8_SB(1, 1), cB + hstep + kstep, voffB);
;         PG8_WAIT_V(6); PG8_BAR;
.LBB0_1324:
	v_ashrrev_i32_e32 v5, 3, v1
	v_lshrrev_b32_e32 v2, 4, v1
	v_and_b32_e32 v3, 8, v0
	v_lshrrev_b32_e32 v7, 2, v5
	v_and_or_b32 v3, v2, 7, v3
	s_mov_b32 s2, 0x1ffff0
	v_and_b32_e32 v7, 4, v7
	s_mov_b32 s4, 0x1fffe0
	v_xor_b32_e32 v2, v2, v0
	v_and_or_b32 v6, v5, s2, v3
	v_and_or_b32 v5, v5, s4, v7
	v_lshlrev_b32_e32 v7, 1, v3
	v_lshlrev_b32_e32 v2, 4, v2
	v_bfe_u32 v4, v1, 4, 2
	v_and_b32_e32 v7, 24, v7
	v_and_b32_e32 v2, 0x70, v2
	v_or3_b32 v5, v5, v7, v4
	v_and_b32_e32 v147, 7, v5
	v_lshlrev_b32_e32 v5, 1, v5
	v_sub_u32_e32 v5, v5, v147
	v_lshl_or_b32 v147, v5, 11, v2
	v_mov_b32_e32 v5, 0x2000
	v_lshl_add_u32 v1, v1, 4, v5
	v_ashrrev_i32_e32 v1, 7, v1
	v_and_or_b32 v3, v1, s2, v3
	v_lshrrev_b32_e32 v5, 2, v1
	s_lshl_b32 s2, s3, 10
	v_and_b32_e32 v5, 4, v5
	s_add_i32 s17, s2, 0
	v_and_or_b32 v1, v1, s4, v5
	s_add_i32 s24, s17, 0x10000
	v_or3_b32 v1, v1, v7, v4
	s_mov_b32 s4, s10
	s_mov_b32 m0, s24
	s_add_i32 s25, s17, 0x12000
	v_and_b32_e32 v5, 7, v1
	v_lshlrev_b32_e32 v149, 1, v1
	v_sub_u32_e32 v149, v149, v5
	v_lshl_or_b32 v149, v149, 11, v2
	s_waitcnt vmcnt(0)
	s_barrier
	buffer_load_dwordx4 v147, s[4:7], s54 offen lds
	s_mov_b32 m0, s25
	s_add_i32 s26, s17, 0x14000
	buffer_load_dwordx4 v149, s[4:7], s54 offen lds
	s_add_i32 s2, s54, 0x4000
	s_mov_b32 m0, s26
	s_add_i32 s27, s17, 0x16000
	buffer_load_dwordx4 v147, s[4:7], s2 offen lds
	s_mov_b32 m0, s27
	v_lshl_or_b32 v146, v6, 11, v2
	buffer_load_dwordx4 v149, s[4:7], s2 offen lds
	s_mov_b32 m0, s17
	s_add_i32 s28, s17, 0x2000
	v_lshl_or_b32 v148, v3, 11, v2
	buffer_load_dwordx4 v146, s[4:7], s53 offen lds
	s_mov_b32 m0, s28
	s_add_i32 s29, s17, 0x4000
	buffer_load_dwordx4 v148, s[4:7], s53 offen lds
	s_add_i32 s2, s53, 0x40000
	s_mov_b32 m0, s29
	s_add_i32 s31, s17, 0x6000
	buffer_load_dwordx4 v146, s[4:7], s2 offen lds
	s_mov_b32 m0, s31
	s_ashr_i32 s16, s14, 8
	buffer_load_dwordx4 v148, s[4:7], s2 offen lds
	s_cmp_eq_u32 s16, 1
	s_cselect_b64 s[10:11], -1, 0
	s_cmp_lg_u32 s16, 1
	s_mov_b32 s2, 0
	s_cbranch_scc1 .LBB0_1326
	s_barrier
.LBB0_1326:
	v_readlane_b32 s44, v254, 2
	v_readlane_b32 s46, v254, 4
	v_readlane_b32 s47, v254, 5
	s_add_u32 s12, s46, 0x85a00000
	s_addc_u32 s13, s47, 0
	s_add_i32 s33, s17, 0x18000
	s_add_i32 s15, s54, 0x80
	s_mov_b32 m0, s33
	s_add_i32 s34, s17, 0x1a000
	s_waitcnt vmcnt(2)
	s_barrier
	buffer_load_dwordx4 v147, s[4:7], s15 offen lds
	s_mov_b32 m0, s34
	s_add_i32 s35, s17, 0x8000
	buffer_load_dwordx4 v149, s[4:7], s15 offen lds
	s_add_i32 s15, s53, 0x80
	s_mov_b32 m0, s35
	s_add_i32 s36, s17, 0xa000
	buffer_load_dwordx4 v146, s[4:7], s15 offen lds
	s_mov_b32 m0, s36
	s_add_i32 s37, s17, 0x1c000
	buffer_load_dwordx4 v148, s[4:7], s15 offen lds
	s_add_i32 s15, s54, 0x4080
	s_mov_b32 m0, s37
	s_add_i32 s38, s17, 0x1e000
	buffer_load_dwordx4 v147, s[4:7], s15 offen lds
	s_mov_b32 m0, s38
	v_lshrrev_b32_e32 v1, 3, v0
	buffer_load_dwordx4 v149, s[4:7], s15 offen lds
	v_and_b32_e32 v3, 7, v0
	v_lshlrev_b32_e32 v0, 4, v0
	v_and_b32_e32 v0, 0x80, v0
	s_and_b32 s4, s3, 3
	v_and_b32_e32 v2, 6, v1
	v_lshl_or_b32 v0, v3, 8, v0
	v_bitop3_b32 v1, v1, v3, 6 bitop3:0x6c
	s_lshl_b32 s15, s16, 13
	s_lshl_b32 s18, s4, 12
	v_lshl_or_b32 v1, v1, 4, v0
	v_or_b32_e32 v4, s15, v1
	v_or_b32_e32 v150, s18, v1
	v_bitop3_b32 v1, v2, v3, 1 bitop3:0x36
	v_lshl_or_b32 v0, v1, 4, v0
	v_or_b32_e32 v1, s15, v0
	s_lshl_b32 s15, s3, 11
	s_add_i32 s39, s15, 0
	s_add_i32 s39, s39, 0x22800
	s_cmp_eq_u32 s3, 4
	s_cselect_b32 s40, 0, 0x400000
	s_add_i32 s41, s17, 0xc000
	s_cmpk_lt_u32 s14, 0x100
	v_or_b32_e32 v151, s18, v0
	s_waitcnt vmcnt(6)
	s_cselect_b64 s[14:15], -1, 0
	s_add_i32 s3, 0, 0x10000
	v_readlane_b32 s45, v254, 3
	v_add_u32_e32 v152, s3, v150
	v_add_u32_e32 v153, s3, v151
	s_add_i32 s3, 0, 0x14000
	s_lshl_b32 s42, s4, 6
	s_lshl_b32 s43, s16, 6
	s_add_i32 s44, s17, 0xe000
	s_add_u32 s45, s46, 0x7d000000
	v_add_u32_e32 v154, s3, v150
	v_add_u32_e32 v155, s3, v151
	v_add_u32_e32 v156, 0, v4
	v_add_u32_e32 v157, 0, v1
	s_mov_b32 s16, 0x3b000000
	s_barrier
	s_branch .LBB0_1329

; #define PG8_STAGE(bufoff, gbase, voff) do { _Pragma("unroll") for (int _i = 0; _i < 2; ++_i) \
;         __builtin_amdgcn_raw_ptr_buffer_load_lds(rsrc, (LAS void*)(lds + (bufoff) + ldsw + _i * 8192), 16, (int)(voff)[_i], (int)(gbase), 0, 0); } while (0)
; #define PG8_STAGE_A(bufoff, h, goff) do { if constexpr (GATHER) { PG8_STAGE(bufoff, goff, vG[h]); } else { PG8_STAGE(bufoff, (goff) + (h) * hstep, voffA); } } while (0)
; #define PG8_WAIT_V(n) asm volatile("s_waitcnt vmcnt(" #n ")" ::: "memory")
; #define PG8_WAIT_L(n) asm volatile("s_waitcnt lgkmcnt(" #n ")" ::: "memory")
; #define PG8_BAR __builtin_amdgcn_s_barrier()
; #define PG8_SCHED __builtin_amdgcn_sched_barrier(0)
;     DI int row_cnt(const pg8::Unit& u) const { return __builtin_amdgcn_readfirstlane(tab[u.a0]) - u.ldc; }
;     ...
;             PG8_LDB(B0, 0, 0); PG8_LDB(B1, 0, 1); PG8_SCHED; PG8_LDA(At, 0, 0); PG8_STAGE_A(PG8_SA(1, 1), 1, a1);
;             if constexpr (GATHER) { if (last && has_next) load_rows((ui + 1) & 1, S.row_cnt(nxt)); }
;             PG8_WAIT_V(8); PG8_WAIT_L(0); PG8_BAR; PG8_MMA(0, 0, At, B0); PG8_MMA(0, 1, At, B1); PG8_BAR; PG8_SCHED;
;             PG8_LDA(At, 0, 1); PG8_STAGE(PG8_SB(0, 0), b2, voffB); PG8_STAGE(PG8_SB(0, 1), b2 + hstep, voffB); PG8_STAGE_A(PG8_SA(0, 0), 0, a2);
;             PG8_WAIT_V(8); PG8_WAIT_L(0); PG8_BAR; PG8_MMA(1, 0, At, B0); PG8_MMA(1, 1, At, B1); PG8_BAR; PG8_SCHED;
;             PG8_LDB(B0, 1, 0); PG8_LDB(B1, 1, 1); PG8_SCHED; PG8_LDA(At, 1, 0); PG8_STAGE_A(PG8_SA(0, 1), 1, a2);
.LBB0_1335:
	s_waitcnt vmcnt(1)
	ds_read_b128 v[128:131], v152
	ds_read_b128 v[136:139], v152 offset:2048
	s_waitcnt vmcnt(0)
	ds_read_b128 v[132:135], v153
	ds_read_b128 v[140:143], v153 offset:2048
	ds_read_b128 v[158:161], v154
	ds_read_b128 v[166:169], v154 offset:2048
	ds_read_b128 v[162:165], v155
	ds_read_b128 v[170:173], v155 offset:2048
	s_add_i32 s4, s3, 0xfffc0080
	s_cmp_eq_u32 s54, 12
	s_cselect_b32 s57, s52, s4
	s_cselect_b32 s56, s51, s53
	s_add_i32 s55, s57, 0x80
	s_mov_b32 s4, s62
	s_mov_b32 m0, s41
	ds_read_b128 v[174:177], v156
	ds_read_b128 v[182:185], v156 offset:2048
	ds_read_b128 v[178:181], v157
	ds_read_b128 v[186:189], v157 offset:2048
	ds_read_b128 v[190:193], v156 offset:4096
	ds_read_b128 v[198:201], v156 offset:6144
	ds_read_b128 v[194:197], v157 offset:4096
	ds_read_b128 v[202:205], v157 offset:6144
	buffer_load_dwordx4 v146, s[4:7], s3 offen lds
	s_mov_b32 m0, s44
	s_nop 0
	buffer_load_dwordx4 v148, s[4:7], s3 offen lds
	s_waitcnt vmcnt(8)
	s_waitcnt lgkmcnt(0)
	s_barrier
	s_setprio 1
	s_waitcnt lgkmcnt(5)
	v_mfma_f32_16x16x128_f8f6f4 v[124:127], v[128:135], v[174:181], v[124:127]
	v_mfma_f32_16x16x128_f8f6f4 v[120:123], v[136:143], v[174:181], v[120:123]
	s_waitcnt lgkmcnt(4)
	v_mfma_f32_16x16x128_f8f6f4 v[108:111], v[128:135], v[182:189], v[108:111]
	v_mfma_f32_16x16x128_f8f6f4 v[104:107], v[136:143], v[182:189], v[104:107]
	s_waitcnt lgkmcnt(1)
	v_mfma_f32_16x16x128_f8f6f4 v[206:209], v[128:135], v[190:197], v[92:95]
	v_mfma_f32_16x16x128_f8f6f4 v[210:213], v[136:143], v[190:197], v[88:91]
	s_waitcnt lgkmcnt(0)
	v_mfma_f32_16x16x128_f8f6f4 v[214:217], v[128:135], v[198:205], v[76:79]
	v_mfma_f32_16x16x128_f8f6f4 v[218:221], v[136:143], v[198:205], v[72:75]
	s_setprio 0
	s_setprio 1
	v_mfma_f32_16x16x128_f8f6f4 v[116:119], v[158:165], v[174:181], v[116:119]
	v_mfma_f32_16x16x128_f8f6f4 v[112:115], v[166:173], v[174:181], v[112:115]
	v_mfma_f32_16x16x128_f8f6f4 v[100:103], v[158:165], v[182:189], v[100:103]
	v_mfma_f32_16x16x128_f8f6f4 v[96:99], v[166:173], v[182:189], v[96:99]
	v_mfma_f32_16x16x128_f8f6f4 v[174:177], v[158:165], v[190:197], v[84:87]
	v_mfma_f32_16x16x128_f8f6f4 v[178:181], v[166:173], v[190:197], v[80:83]
	v_mfma_f32_16x16x128_f8f6f4 v[182:185], v[158:165], v[198:205], v[68:71]
	v_mfma_f32_16x16x128_f8f6f4 v[186:189], v[166:173], v[198:205], v[64:67]
	s_setprio 0
	s_barrier
	s_mov_b32 m0, s24
	s_nop 3
	ds_read_b128 v[64:67], v156 offset:16384
	ds_read_b128 v[72:75], v156 offset:18432
	ds_read_b128 v[68:71], v157 offset:16384
	ds_read_b128 v[76:79], v157 offset:18432
	ds_read_b128 v[80:83], v156 offset:20480
	ds_read_b128 v[88:91], v156 offset:22528
	ds_read_b128 v[84:87], v157 offset:20480
	ds_read_b128 v[92:95], v157 offset:22528
	buffer_load_dwordx4 v147, s[4:7], s56 offen lds
	s_mov_b32 m0, s25
	s_add_i32 s58, s56, 0x4000
	buffer_load_dwordx4 v149, s[4:7], s56 offen lds
	s_mov_b32 m0, s26
	s_nop 0
	buffer_load_dwordx4 v147, s[4:7], s58 offen lds
	s_mov_b32 m0, s27
	s_nop 0
	buffer_load_dwordx4 v149, s[4:7], s58 offen lds
	s_mov_b32 m0, s17
	s_nop 0
	buffer_load_dwordx4 v146, s[4:7], s57 offen lds
	s_mov_b32 m0, s28
	s_nop 0
	buffer_load_dwordx4 v148, s[4:7], s57 offen lds
	s_waitcnt vmcnt(8)
	s_waitcnt lgkmcnt(0)
	s_barrier
	s_setprio 1
	s_waitcnt lgkmcnt(5)
	v_mfma_f32_16x16x128_f8f6f4 v[60:63], v[128:135], v[64:71], v[60:63]
	v_mfma_f32_16x16x128_f8f6f4 v[56:59], v[136:143], v[64:71], v[56:59]
	s_waitcnt lgkmcnt(4)
	v_mfma_f32_16x16x128_f8f6f4 v[190:193], v[128:135], v[72:79], v[44:47]
	v_mfma_f32_16x16x128_f8f6f4 v[194:197], v[136:143], v[72:79], v[40:43]
	s_waitcnt lgkmcnt(1)
	v_mfma_f32_16x16x128_f8f6f4 v[198:201], v[128:135], v[80:87], v[28:31]
	v_mfma_f32_16x16x128_f8f6f4 v[202:205], v[136:143], v[80:87], v[24:27]
	s_waitcnt lgkmcnt(0)
	v_mfma_f32_16x16x128_f8f6f4 v[222:225], v[128:135], v[88:95], v[12:15]
	v_mfma_f32_16x16x128_f8f6f4 v[226:229], v[136:143], v[88:95], v[8:11]
	s_setprio 0
	s_setprio 1
	v_mfma_f32_16x16x128_f8f6f4 v[52:55], v[158:165], v[64:71], v[52:55]
	v_mfma_f32_16x16x128_f8f6f4 v[48:51], v[166:173], v[64:71], v[48:51]
	v_mfma_f32_16x16x128_f8f6f4 v[230:233], v[158:165], v[72:79], v[36:39]
	v_mfma_f32_16x16x128_f8f6f4 v[234:237], v[166:173], v[72:79], v[32:35]
	v_mfma_f32_16x16x128_f8f6f4 v[238:241], v[158:165], v[80:87], v[20:23]
	v_mfma_f32_16x16x128_f8f6f4 v[242:245], v[166:173], v[80:87], v[16:19]
	v_mfma_f32_16x16x128_f8f6f4 v[246:249], v[158:165], v[88:95], v[4:7]
	v_mfma_f32_16x16x128_f8f6f4 v[250:253], v[166:173], v[88:95], v[0:3]
	s_setprio 0
	s_barrier
	s_add_i32 s58, 0, 0x18000
	s_nop 2
	v_add_u32_e32 v4, s58, v150
	v_add_u32_e32 v8, s58, v151
	s_add_i32 s58, 0, 0x1c000
	ds_read_b128 v[0:3], v4
	ds_read_b128 v[16:19], v4 offset:2048
	ds_read_b128 v[4:7], v8
	ds_read_b128 v[20:23], v8 offset:2048
	v_add_u32_e32 v8, s58, v150
	v_add_u32_e32 v9, s58, v151
	ds_read_b128 v[128:131], v8
	ds_read_b128 v[136:139], v8 offset:2048
	ds_read_b128 v[132:135], v9
	ds_read_b128 v[140:143], v9 offset:2048
	s_add_i32 s57, s57, 0x40000
	s_mov_b32 m0, s29
	ds_read_b128 v[8:11], v156 offset:32768
	ds_read_b128 v[24:27], v156 offset:34816
	ds_read_b128 v[12:15], v157 offset:32768
	ds_read_b128 v[28:31], v157 offset:34816
	ds_read_b128 v[32:35], v156 offset:36864
	ds_read_b128 v[40:43], v156 offset:38912
	ds_read_b128 v[36:39], v157 offset:36864
	ds_read_b128 v[44:47], v157 offset:38912
	buffer_load_dwordx4 v146, s[4:7], s57 offen lds
	s_mov_b32 m0, s31
	s_nop 0
	buffer_load_dwordx4 v148, s[4:7], s57 offen lds
	s_waitcnt vmcnt(8)
	s_waitcnt lgkmcnt(0)
	s_barrier
; DI unsigned pk4f8(float a, float b, float c, float d) { int p = __builtin_amdgcn_cvt_pk_fp8_f32(a, b, 0, false); p = __builtin_amdgcn_cvt_pk_fp8_f32(c, d, p, true); return (unsigned)p; }
; #define PG8_STAGE(bufoff, gbase, voff) do { _Pragma("unroll") for (int _i = 0; _i < 2; ++_i) \
;         __builtin_amdgcn_raw_ptr_buffer_load_lds(rsrc, (LAS void*)(lds + (bufoff) + ldsw + _i * 8192), 16, (int)(voff)[_i], (int)(gbase), 0, 0); } while (0)
; #define PG8_STAGE_A(bufoff, h, goff) do { if constexpr (GATHER) { PG8_STAGE(bufoff, goff, vG[h]); } else { PG8_STAGE(bufoff, (goff) + (h) * hstep, voffA); } } while (0)
; #define PG8_WAIT_V(n) asm volatile("s_waitcnt vmcnt(" #n ")" ::: "memory")
; #define PG8_BAR __builtin_amdgcn_s_barrier()
;     ...
;             PG8_LDB(B0, 1, 0); PG8_LDB(B1, 1, 1); PG8_SCHED; PG8_LDA(At, 1, 0); PG8_STAGE_A(PG8_SA(0, 1), 1, a2);
;             PG8_WAIT_V(8); PG8_WAIT_L(0); PG8_BAR; PG8_MMA(0, 0, At, B0); PG8_MMA(0, 1, At, B1); PG8_BAR; PG8_SCHED;
;             PG8_LDA(At, 1, 1); PG8_STAGE(PG8_SB(1, 0), b3, voffB); PG8_STAGE(PG8_SB(1, 1), b3 + hstep, voffB); PG8_STAGE_A(PG8_SA(1, 0), 0, a3);
;             PG8_WAIT_V(8); PG8_WAIT_L(0); PG8_BAR; PG8_MMA(1, 0, At, B0); PG8_MMA(1, 1, At, B1); PG8_BAR; PG8_SCHED;
;     __device__ __forceinline__ void operator()(const f32x4 (&acc)[2][2][4][2], const Unit& u, int wr, int wc, int fr, int fq) const {
;     ...
;         const int col0 = u.a1 * BM + wc * 32 + 8 * fq; const float* bp = bdn + (size_t)u.a0 * D + col0;
;         f32x4 bv[2][2];
; #pragma unroll
;         for (int bj = 0; bj < 2; ++bj)
; #pragma unroll
;             for (int n = 0; n < 2; ++n) bv[bj][n] = *(const f32x4*)(bp + bj * HALF + 4 * n);
;         const int row0 = wr * 64 + fr;
; #pragma unroll
;         for (int ai = 0; ai < 2; ++ai)
; #pragma unroll
;             for (int m = 0; m < 4; ++m) { const int r = row0 + ai * HALF + m * 16;
;                 if (r < valid) { const int slot = slots[r]; const float w = wts[r]; unsigned char* rowp = ys + (size_t)slot * D + col0;
; #pragma unroll
;                     for (int bj = 0; bj < 2; ++bj) { const f32x4 v0 = (acc[ai][bj][m][0] * WSCALE_INV + bv[bj][0]) * w, v1 = (acc[ai][bj][m][1] * WSCALE_INV + bv[bj][1]) * w;
;                         u32x2 o; o.x = pk4f8(v0[0], v0[1], v0[2], v0[3]); o.y = pk4f8(v1[0], v1[1], v1[2], v1[3]);
;                         *(u32x2*)(rowp + bj * HALF) = o; } } }
	s_setprio 1
	s_waitcnt lgkmcnt(5)
	v_mfma_f32_16x16x128_f8f6f4 v[124:127], v[0:7], v[8:15], v[124:127]
	v_mfma_f32_16x16x128_f8f6f4 v[120:123], v[16:23], v[8:15], v[120:123]
	s_waitcnt lgkmcnt(4)
	v_mfma_f32_16x16x128_f8f6f4 v[108:111], v[0:7], v[24:31], v[108:111]
	v_mfma_f32_16x16x128_f8f6f4 v[104:107], v[16:23], v[24:31], v[104:107]
	s_waitcnt lgkmcnt(1)
	v_mfma_f32_16x16x128_f8f6f4 v[92:95], v[0:7], v[32:39], v[206:209]
	v_mfma_f32_16x16x128_f8f6f4 v[88:91], v[16:23], v[32:39], v[210:213]
	s_waitcnt lgkmcnt(0)
	v_mfma_f32_16x16x128_f8f6f4 v[76:79], v[0:7], v[40:47], v[214:217]
	v_mfma_f32_16x16x128_f8f6f4 v[72:75], v[16:23], v[40:47], v[218:221]
	s_setprio 0
	s_setprio 1
	v_mfma_f32_16x16x128_f8f6f4 v[116:119], v[128:135], v[8:15], v[116:119]
	v_mfma_f32_16x16x128_f8f6f4 v[112:115], v[136:143], v[8:15], v[112:115]
	v_mfma_f32_16x16x128_f8f6f4 v[100:103], v[128:135], v[24:31], v[100:103]
	v_mfma_f32_16x16x128_f8f6f4 v[96:99], v[136:143], v[24:31], v[96:99]
	v_mfma_f32_16x16x128_f8f6f4 v[84:87], v[128:135], v[32:39], v[174:177]
	v_mfma_f32_16x16x128_f8f6f4 v[80:83], v[136:143], v[32:39], v[178:181]
	v_mfma_f32_16x16x128_f8f6f4 v[68:71], v[128:135], v[40:47], v[182:185]
	v_mfma_f32_16x16x128_f8f6f4 v[64:67], v[136:143], v[40:47], v[186:189]
	s_setprio 0
	s_barrier
	s_mov_b32 m0, s33
	s_add_i32 s57, s56, 0x80
	ds_read_b128 v[32:35], v156 offset:49152
	ds_read_b128 v[158:161], v156 offset:51200
	ds_read_b128 v[36:39], v157 offset:49152
	ds_read_b128 v[162:165], v157 offset:51200
	ds_read_b128 v[166:169], v156 offset:53248
	ds_read_b128 v[174:177], v156 offset:55296
	ds_read_b128 v[170:173], v157 offset:53248
	ds_read_b128 v[178:181], v157 offset:55296
	buffer_load_dwordx4 v147, s[4:7], s57 offen lds
	s_mov_b32 m0, s34
	s_add_i32 s56, s56, 0x4080
	buffer_load_dwordx4 v149, s[4:7], s57 offen lds
	s_mov_b32 m0, s37
	s_nop 0
	buffer_load_dwordx4 v147, s[4:7], s56 offen lds
	s_mov_b32 m0, s38
	s_nop 0
	buffer_load_dwordx4 v149, s[4:7], s56 offen lds
	s_mov_b32 m0, s35
	s_nop 0
	buffer_load_dwordx4 v146, s[4:7], s55 offen lds
	s_mov_b32 m0, s36
	s_nop 0
	buffer_load_dwordx4 v148, s[4:7], s55 offen lds
	s_waitcnt vmcnt(8)
	s_waitcnt lgkmcnt(0)
	s_barrier
	s_setprio 1
	s_waitcnt lgkmcnt(5)
	v_mfma_f32_16x16x128_f8f6f4 v[60:63], v[0:7], v[32:39], v[60:63]
	v_mfma_f32_16x16x128_f8f6f4 v[56:59], v[16:23], v[32:39], v[56:59]
	s_waitcnt lgkmcnt(4)
	v_mfma_f32_16x16x128_f8f6f4 v[44:47], v[0:7], v[158:165], v[190:193]
	v_mfma_f32_16x16x128_f8f6f4 v[40:43], v[16:23], v[158:165], v[194:197]
	s_waitcnt lgkmcnt(1)
	v_mfma_f32_16x16x128_f8f6f4 v[28:31], v[0:7], v[166:173], v[198:201]
	v_mfma_f32_16x16x128_f8f6f4 v[24:27], v[16:23], v[166:173], v[202:205]
	s_waitcnt lgkmcnt(0)
	v_mfma_f32_16x16x128_f8f6f4 v[12:15], v[0:7], v[174:181], v[222:225]
	v_mfma_f32_16x16x128_f8f6f4 v[8:11], v[16:23], v[174:181], v[226:229]
	s_setprio 0
	s_setprio 1
	v_mfma_f32_16x16x128_f8f6f4 v[52:55], v[128:135], v[32:39], v[52:55]
	v_mfma_f32_16x16x128_f8f6f4 v[48:51], v[136:143], v[32:39], v[48:51]
	v_mfma_f32_16x16x128_f8f6f4 v[36:39], v[128:135], v[158:165], v[230:233]
	v_mfma_f32_16x16x128_f8f6f4 v[32:35], v[136:143], v[158:165], v[234:237]
	v_mfma_f32_16x16x128_f8f6f4 v[20:23], v[128:135], v[166:173], v[238:241]
	v_mfma_f32_16x16x128_f8f6f4 v[16:19], v[136:143], v[166:173], v[242:245]
	v_mfma_f32_16x16x128_f8f6f4 v[4:7], v[128:135], v[174:181], v[246:249]
	v_mfma_f32_16x16x128_f8f6f4 v[0:3], v[136:143], v[174:181], v[250:253]
	s_setprio 0
	s_barrier
	s_add_i32 s54, s54, 2
	s_addk_i32 s3, 0x100
	s_addk_i32 s53, 0x100
	s_cmp_gt_u32 s54, 13
	s_cbranch_scc0 .LBB0_1335
	s_and_b64 vcc, exec, s[14:15]
	s_cbranch_vccz .LBB0_1338
	s_barrier
.LBB0_1338:
	s_lshl_b32 s2, s2, 10
	v_mbcnt_lo_u32_b32 v158, -1, 0
	v_mbcnt_hi_u32_b32 v158, -1, v158
	s_and_b32 s2, s2, 0x400
	s_add_i32 s4, s2, 0
	s_lshl_b32 s2, s23, 8
	v_and_b32_e32 v128, 48, v158
	v_readlane_b32 s56, v254, 6
	s_or_b32 s2, s2, s42
	s_ashr_i32 s23, s22, 31
	v_readlane_b32 s57, v254, 7
	v_readlane_b32 s58, v254, 8
	v_readlane_b32 s59, v254, 9
	v_readlane_b32 s60, v254, 10
	v_readlane_b32 s61, v254, 11
	s_add_i32 s53, s4, 0x24800
	v_add_u32_e32 v144, s2, v128
	s_lshl_b64 s[2:3], s[22:23], 13
	v_readlane_b32 s62, v254, 12
	v_readlane_b32 s63, v254, 13
	s_mov_b64 s[56:57], s[60:61]
	s_add_u32 s2, s56, s2
	s_addc_u32 s3, s57, s3
	v_ashrrev_i32_e32 v145, 31, v144
	v_lshl_add_u64 v[132:133], v[144:145], 2, s[2:3]
	global_load_dwordx4 v[136:139], v[132:133], off offset:16
	global_load_dwordx4 v[140:143], v[132:133], off
	global_load_dwordx4 v[128:131], v[132:133], off offset:48
	s_nop 0
	global_load_dwordx4 v[132:135], v[132:133], off offset:32
	v_and_or_b32 v160, v158, 15, s43
	s_add_i32 s4, s4, 0x25000
	v_lshlrev_b32_e32 v158, 2, v160
	v_cmp_gt_i32_e32 vcc, s30, v160
	v_add_u32_e32 v159, s53, v158
	v_add_u32_e32 v158, s4, v158
	s_mov_b64 s[58:59], s[62:63]
	s_and_saveexec_b64 s[2:3], vcc
	s_cbranch_execz .LBB0_1340
	ds_read_b32 v162, v159
	ds_read_b32 v164, v158
	s_waitcnt vmcnt(3)
	v_pk_fma_f32 v[120:121], v[120:121], s[16:17], v[136:137] op_sel_hi:[1,0,1]
	v_mov_b32_e32 v167, 0
	s_waitcnt vmcnt(2)
	v_pk_fma_f32 v[124:125], v[124:125], s[16:17], v[140:141] op_sel_hi:[1,0,1]
	v_mov_b32_e32 v166, 0
	s_waitcnt lgkmcnt(0)
	v_pk_mul_f32 v[120:121], v[120:121], v[164:165] op_sel_hi:[1,0]
	v_pk_mul_f32 v[124:125], v[124:125], v[164:165] op_sel_hi:[1,0]
	v_cvt_pk_fp8_f32 v167, v120, v121
	v_pk_fma_f32 v[120:121], v[122:123], s[16:17], v[138:139] op_sel_hi:[1,0,1]
	s_waitcnt vmcnt(0)
	v_pk_fma_f32 v[116:117], v[116:117], s[16:17], v[132:133] op_sel_hi:[1,0,1]
	v_pk_mul_f32 v[120:121], v[120:121], v[164:165] op_sel_hi:[1,0]
	v_pk_fma_f32 v[112:113], v[112:113], s[16:17], v[128:129] op_sel_hi:[1,0,1]
	v_cvt_pk_fp8_f32 v166, v124, v125
	v_cvt_pk_fp8_f32 v167, v120, v121 op_sel:[0,0,1]
	v_pk_mul_f32 v[116:117], v[116:117], v[164:165] op_sel_hi:[1,0]
	v_pk_mul_f32 v[112:113], v[112:113], v[164:165] op_sel_hi:[1,0]
	v_mov_b32_e32 v168, 0
	v_mov_b32_e32 v169, 0
	v_cvt_pk_fp8_f32 v168, v116, v117
	v_cvt_pk_fp8_f32 v169, v112, v113
	v_pk_fma_f32 v[126:127], v[126:127], s[16:17], v[142:143] op_sel_hi:[1,0,1]
	v_pk_fma_f32 v[118:119], v[118:119], s[16:17], v[134:135] op_sel_hi:[1,0,1]
	v_pk_mul_f32 v[126:127], v[126:127], v[164:165] op_sel_hi:[1,0]
	v_pk_fma_f32 v[112:113], v[114:115], s[16:17], v[130:131] op_sel_hi:[1,0,1]
	v_ashrrev_i32_e32 v163, 31, v162
	v_cvt_pk_fp8_f32 v166, v126, v127 op_sel:[0,0,1]
	v_pk_mul_f32 v[118:119], v[118:119], v[164:165] op_sel_hi:[1,0]
	v_pk_mul_f32 v[112:113], v[112:113], v[164:165] op_sel_hi:[1,0]
	v_lshlrev_b64 v[162:163], 11, v[162:163]
	v_cvt_pk_fp8_f32 v168, v118, v119 op_sel:[0,0,1]
	v_cvt_pk_fp8_f32 v169, v112, v113 op_sel:[0,0,1]
	v_lshl_add_u64 v[112:113], s[12:13], 0, v[162:163]
	v_lshl_add_u64 v[112:113], v[112:113], 0, v[144:145]
	global_store_dwordx4 v[112:113], v[166:169], off
; DI unsigned pk4f8(float a, float b, float c, float d) { int p = __builtin_amdgcn_cvt_pk_fp8_f32(a, b, 0, false); p = __builtin_amdgcn_cvt_pk_fp8_f32(c, d, p, true); return (unsigned)p; }
;     __device__ __forceinline__ void operator()(const f32x4 (&acc)[2][2][4][2], const Unit& u, int wr, int wc, int fr, int fq) const {
;     ...
;             for (int m = 0; m < 4; ++m) { const int r = row0 + ai * HALF + m * 16;
;                 if (r < valid) { const int slot = slots[r]; const float w = wts[r]; unsigned char* rowp = ys + (size_t)slot * D + col0;
; #pragma unroll
;                     for (int bj = 0; bj < 2; ++bj) { const f32x4 v0 = (acc[ai][bj][m][0] * WSCALE_INV + bv[bj][0]) * w, v1 = (acc[ai][bj][m][1] * WSCALE_INV + bv[bj][1]) * w;
;                         u32x2 o; o.x = pk4f8(v0[0], v0[1], v0[2], v0[3]); o.y = pk4f8(v1[0], v1[1], v1[2], v1[3]);
;                         *(u32x2*)(rowp + bj * HALF) = o; } } }
.LBB0_1340:
	s_or_b64 exec, exec, s[2:3]
	v_or_b32_e32 v112, 16, v160
	v_cmp_gt_i32_e32 vcc, s30, v112
	s_and_saveexec_b64 s[2:3], vcc
	s_cbranch_execz .LBB0_1342
	ds_read_b32 v112, v159 offset:64
	ds_read_b32 v114, v158 offset:64
	v_pk_fma_f32 v[104:105], v[104:105], s[16:17], v[136:137] op_sel_hi:[1,0,1]
	v_mov_b32_e32 v167, 0
	v_pk_fma_f32 v[108:109], v[108:109], s[16:17], v[140:141] op_sel_hi:[1,0,1]
	v_mov_b32_e32 v166, 0
	s_waitcnt lgkmcnt(0)
	v_pk_mul_f32 v[104:105], v[104:105], v[114:115] op_sel_hi:[1,0]
	v_pk_mul_f32 v[108:109], v[108:109], v[114:115] op_sel_hi:[1,0]
	v_cvt_pk_fp8_f32 v167, v104, v105
	v_pk_fma_f32 v[104:105], v[106:107], s[16:17], v[138:139] op_sel_hi:[1,0,1]
	v_pk_fma_f32 v[100:101], v[100:101], s[16:17], v[132:133] op_sel_hi:[1,0,1]
	v_pk_mul_f32 v[104:105], v[104:105], v[114:115] op_sel_hi:[1,0]
	v_pk_fma_f32 v[96:97], v[96:97], s[16:17], v[128:129] op_sel_hi:[1,0,1]
	v_cvt_pk_fp8_f32 v166, v108, v109
	v_cvt_pk_fp8_f32 v167, v104, v105 op_sel:[0,0,1]
	v_pk_mul_f32 v[100:101], v[100:101], v[114:115] op_sel_hi:[1,0]
	v_pk_mul_f32 v[96:97], v[96:97], v[114:115] op_sel_hi:[1,0]
	v_mov_b32_e32 v168, 0
	v_mov_b32_e32 v169, 0
	v_cvt_pk_fp8_f32 v168, v100, v101
	v_cvt_pk_fp8_f32 v169, v96, v97
	v_pk_fma_f32 v[110:111], v[110:111], s[16:17], v[142:143] op_sel_hi:[1,0,1]
	v_pk_fma_f32 v[102:103], v[102:103], s[16:17], v[134:135] op_sel_hi:[1,0,1]
	v_pk_mul_f32 v[110:111], v[110:111], v[114:115] op_sel_hi:[1,0]
	v_pk_fma_f32 v[96:97], v[98:99], s[16:17], v[130:131] op_sel_hi:[1,0,1]
	v_ashrrev_i32_e32 v113, 31, v112
	v_cvt_pk_fp8_f32 v166, v110, v111 op_sel:[0,0,1]
	v_pk_mul_f32 v[102:103], v[102:103], v[114:115] op_sel_hi:[1,0]
	v_pk_mul_f32 v[96:97], v[96:97], v[114:115] op_sel_hi:[1,0]
	v_lshlrev_b64 v[112:113], 11, v[112:113]
	v_cvt_pk_fp8_f32 v168, v102, v103 op_sel:[0,0,1]
	v_cvt_pk_fp8_f32 v169, v96, v97 op_sel:[0,0,1]
	v_lshl_add_u64 v[96:97], s[12:13], 0, v[112:113]
	v_lshl_add_u64 v[96:97], v[96:97], 0, v[144:145]
	global_store_dwordx4 v[96:97], v[166:169], off
.LBB0_1342:
	s_or_b64 exec, exec, s[2:3]
	v_or_b32_e32 v96, 32, v160
	v_cmp_gt_i32_e32 vcc, s30, v96
	s_and_saveexec_b64 s[2:3], vcc
	s_cbranch_execz .LBB0_1344
	ds_read_b32 v96, v159 offset:128
	ds_read_b32 v98, v158 offset:128
	v_pk_fma_f32 v[88:89], v[88:89], s[16:17], v[136:137] op_sel_hi:[1,0,1]
	v_mov_b32_e32 v167, 0
	v_pk_fma_f32 v[92:93], v[92:93], s[16:17], v[140:141] op_sel_hi:[1,0,1]
	v_mov_b32_e32 v166, 0
	s_waitcnt lgkmcnt(0)
	v_pk_mul_f32 v[88:89], v[88:89], v[98:99] op_sel_hi:[1,0]
	v_pk_mul_f32 v[92:93], v[92:93], v[98:99] op_sel_hi:[1,0]
	v_cvt_pk_fp8_f32 v167, v88, v89
	v_pk_fma_f32 v[88:89], v[90:91], s[16:17], v[138:139] op_sel_hi:[1,0,1]
	v_pk_fma_f32 v[84:85], v[84:85], s[16:17], v[132:133] op_sel_hi:[1,0,1]
	v_pk_mul_f32 v[88:89], v[88:89], v[98:99] op_sel_hi:[1,0]
	v_pk_fma_f32 v[80:81], v[80:81], s[16:17], v[128:129] op_sel_hi:[1,0,1]
	v_cvt_pk_fp8_f32 v166, v92, v93
	v_cvt_pk_fp8_f32 v167, v88, v89 op_sel:[0,0,1]
	v_pk_mul_f32 v[84:85], v[84:85], v[98:99] op_sel_hi:[1,0]
	v_pk_mul_f32 v[80:81], v[80:81], v[98:99] op_sel_hi:[1,0]
	v_mov_b32_e32 v168, 0
	v_mov_b32_e32 v169, 0
	v_cvt_pk_fp8_f32 v168, v84, v85
	v_cvt_pk_fp8_f32 v169, v80, v81
	v_pk_fma_f32 v[94:95], v[94:95], s[16:17], v[142:143] op_sel_hi:[1,0,1]
	v_pk_fma_f32 v[86:87], v[86:87], s[16:17], v[134:135] op_sel_hi:[1,0,1]
	v_pk_mul_f32 v[94:95], v[94:95], v[98:99] op_sel_hi:[1,0]
	v_pk_fma_f32 v[80:81], v[82:83], s[16:17], v[130:131] op_sel_hi:[1,0,1]
	v_ashrrev_i32_e32 v97, 31, v96
	v_cvt_pk_fp8_f32 v166, v94, v95 op_sel:[0,0,1]
	v_pk_mul_f32 v[86:87], v[86:87], v[98:99] op_sel_hi:[1,0]
	v_pk_mul_f32 v[80:81], v[80:81], v[98:99] op_sel_hi:[1,0]
	v_lshlrev_b64 v[96:97], 11, v[96:97]
	v_cvt_pk_fp8_f32 v168, v86, v87 op_sel:[0,0,1]
	v_cvt_pk_fp8_f32 v169, v80, v81 op_sel:[0,0,1]
	v_lshl_add_u64 v[80:81], s[12:13], 0, v[96:97]
	v_lshl_add_u64 v[80:81], v[80:81], 0, v[144:145]
	global_store_dwordx4 v[80:81], v[166:169], off
.LBB0_1344:
	s_or_b64 exec, exec, s[2:3]
	v_or_b32_e32 v80, 48, v160
	v_cmp_gt_i32_e32 vcc, s30, v80
	s_and_saveexec_b64 s[2:3], vcc
	s_cbranch_execz .LBB0_1346
	ds_read_b32 v80, v159 offset:192
	ds_read_b32 v82, v158 offset:192
	v_pk_fma_f32 v[72:73], v[72:73], s[16:17], v[136:137] op_sel_hi:[1,0,1]
	v_mov_b32_e32 v167, 0
	v_pk_fma_f32 v[76:77], v[76:77], s[16:17], v[140:141] op_sel_hi:[1,0,1]
	v_mov_b32_e32 v166, 0
	s_waitcnt lgkmcnt(0)
	v_pk_mul_f32 v[72:73], v[72:73], v[82:83] op_sel_hi:[1,0]
	v_pk_mul_f32 v[76:77], v[76:77], v[82:83] op_sel_hi:[1,0]
	v_cvt_pk_fp8_f32 v167, v72, v73
	v_pk_fma_f32 v[72:73], v[74:75], s[16:17], v[138:139] op_sel_hi:[1,0,1]
	v_pk_fma_f32 v[68:69], v[68:69], s[16:17], v[132:133] op_sel_hi:[1,0,1]
	v_pk_mul_f32 v[72:73], v[72:73], v[82:83] op_sel_hi:[1,0]
	v_pk_fma_f32 v[64:65], v[64:65], s[16:17], v[128:129] op_sel_hi:[1,0,1]
	v_cvt_pk_fp8_f32 v166, v76, v77
	v_cvt_pk_fp8_f32 v167, v72, v73 op_sel:[0,0,1]
	v_pk_mul_f32 v[68:69], v[68:69], v[82:83] op_sel_hi:[1,0]
	v_pk_mul_f32 v[64:65], v[64:65], v[82:83] op_sel_hi:[1,0]
	v_mov_b32_e32 v168, 0
	v_mov_b32_e32 v169, 0
	v_cvt_pk_fp8_f32 v168, v68, v69
	v_cvt_pk_fp8_f32 v169, v64, v65
	v_pk_fma_f32 v[78:79], v[78:79], s[16:17], v[142:143] op_sel_hi:[1,0,1]
	v_pk_fma_f32 v[70:71], v[70:71], s[16:17], v[134:135] op_sel_hi:[1,0,1]
	v_pk_mul_f32 v[78:79], v[78:79], v[82:83] op_sel_hi:[1,0]
	v_pk_fma_f32 v[64:65], v[66:67], s[16:17], v[130:131] op_sel_hi:[1,0,1]
	v_ashrrev_i32_e32 v81, 31, v80
	v_cvt_pk_fp8_f32 v166, v78, v79 op_sel:[0,0,1]
	v_pk_mul_f32 v[70:71], v[70:71], v[82:83] op_sel_hi:[1,0]
	v_pk_mul_f32 v[64:65], v[64:65], v[82:83] op_sel_hi:[1,0]
	v_lshlrev_b64 v[80:81], 11, v[80:81]
	v_cvt_pk_fp8_f32 v168, v70, v71 op_sel:[0,0,1]
	v_cvt_pk_fp8_f32 v169, v64, v65 op_sel:[0,0,1]
	v_lshl_add_u64 v[64:65], s[12:13], 0, v[80:81]
	v_lshl_add_u64 v[64:65], v[64:65], 0, v[144:145]
	global_store_dwordx4 v[64:65], v[166:169], off
; DI unsigned pk4f8(float a, float b, float c, float d) { int p = __builtin_amdgcn_cvt_pk_fp8_f32(a, b, 0, false); p = __builtin_amdgcn_cvt_pk_fp8_f32(c, d, p, true); return (unsigned)p; }
;     __device__ __forceinline__ void operator()(const f32x4 (&acc)[2][2][4][2], const Unit& u, int wr, int wc, int fr, int fq) const {
;     ...
;             for (int m = 0; m < 4; ++m) { const int r = row0 + ai * HALF + m * 16;
;                 if (r < valid) { const int slot = slots[r]; const float w = wts[r]; unsigned char* rowp = ys + (size_t)slot * D + col0;
; #pragma unroll
;                     for (int bj = 0; bj < 2; ++bj) { const f32x4 v0 = (acc[ai][bj][m][0] * WSCALE_INV + bv[bj][0]) * w, v1 = (acc[ai][bj][m][1] * WSCALE_INV + bv[bj][1]) * w;
;                         u32x2 o; o.x = pk4f8(v0[0], v0[1], v0[2], v0[3]); o.y = pk4f8(v1[0], v1[1], v1[2], v1[3]);
;                         *(u32x2*)(rowp + bj * HALF) = o; } } }
.LBB0_1346:
	s_or_b64 exec, exec, s[2:3]
	v_add_u32_e32 v64, 0x80, v160
	v_cmp_gt_i32_e32 vcc, s30, v64
	s_and_saveexec_b64 s[2:3], vcc
	s_cbranch_execz .LBB0_1348
	ds_read_b32 v64, v159 offset:512
	ds_read_b32 v66, v158 offset:512
	v_pk_fma_f32 v[56:57], v[56:57], s[16:17], v[136:137] op_sel_hi:[1,0,1]
	v_mov_b32_e32 v167, 0
	v_pk_fma_f32 v[60:61], v[60:61], s[16:17], v[140:141] op_sel_hi:[1,0,1]
	v_mov_b32_e32 v166, 0
	s_waitcnt lgkmcnt(0)
	v_pk_mul_f32 v[56:57], v[56:57], v[66:67] op_sel_hi:[1,0]
	v_pk_mul_f32 v[60:61], v[60:61], v[66:67] op_sel_hi:[1,0]
	v_cvt_pk_fp8_f32 v167, v56, v57
	v_pk_fma_f32 v[56:57], v[58:59], s[16:17], v[138:139] op_sel_hi:[1,0,1]
	v_pk_fma_f32 v[52:53], v[52:53], s[16:17], v[132:133] op_sel_hi:[1,0,1]
	v_pk_mul_f32 v[56:57], v[56:57], v[66:67] op_sel_hi:[1,0]
	v_pk_fma_f32 v[48:49], v[48:49], s[16:17], v[128:129] op_sel_hi:[1,0,1]
	v_cvt_pk_fp8_f32 v166, v60, v61
	v_cvt_pk_fp8_f32 v167, v56, v57 op_sel:[0,0,1]
	v_pk_mul_f32 v[52:53], v[52:53], v[66:67] op_sel_hi:[1,0]
	v_pk_mul_f32 v[48:49], v[48:49], v[66:67] op_sel_hi:[1,0]
	v_mov_b32_e32 v168, 0
	v_mov_b32_e32 v169, 0
	v_cvt_pk_fp8_f32 v168, v52, v53
	v_cvt_pk_fp8_f32 v169, v48, v49
	v_pk_fma_f32 v[62:63], v[62:63], s[16:17], v[142:143] op_sel_hi:[1,0,1]
	v_pk_fma_f32 v[54:55], v[54:55], s[16:17], v[134:135] op_sel_hi:[1,0,1]
	v_pk_mul_f32 v[62:63], v[62:63], v[66:67] op_sel_hi:[1,0]
	v_pk_fma_f32 v[48:49], v[50:51], s[16:17], v[130:131] op_sel_hi:[1,0,1]
	v_ashrrev_i32_e32 v65, 31, v64
	v_cvt_pk_fp8_f32 v166, v62, v63 op_sel:[0,0,1]
	v_pk_mul_f32 v[54:55], v[54:55], v[66:67] op_sel_hi:[1,0]
	v_pk_mul_f32 v[48:49], v[48:49], v[66:67] op_sel_hi:[1,0]
	v_lshlrev_b64 v[64:65], 11, v[64:65]
	v_cvt_pk_fp8_f32 v168, v54, v55 op_sel:[0,0,1]
	v_cvt_pk_fp8_f32 v169, v48, v49 op_sel:[0,0,1]
	v_lshl_add_u64 v[48:49], s[12:13], 0, v[64:65]
	v_lshl_add_u64 v[48:49], v[48:49], 0, v[144:145]
	global_store_dwordx4 v[48:49], v[166:169], off
.LBB0_1348:
	s_or_b64 exec, exec, s[2:3]
	v_add_u32_e32 v48, 0x90, v160
	v_cmp_gt_i32_e32 vcc, s30, v48
	s_and_saveexec_b64 s[2:3], vcc
	s_cbranch_execz .LBB0_1350
	ds_read_b32 v48, v159 offset:576
	ds_read_b32 v50, v158 offset:576
	v_pk_fma_f32 v[40:41], v[40:41], s[16:17], v[136:137] op_sel_hi:[1,0,1]
	v_mov_b32_e32 v167, 0
	v_pk_fma_f32 v[44:45], v[44:45], s[16:17], v[140:141] op_sel_hi:[1,0,1]
	v_mov_b32_e32 v166, 0
	s_waitcnt lgkmcnt(0)
	v_pk_mul_f32 v[40:41], v[40:41], v[50:51] op_sel_hi:[1,0]
	v_pk_mul_f32 v[44:45], v[44:45], v[50:51] op_sel_hi:[1,0]
	v_cvt_pk_fp8_f32 v167, v40, v41
	v_pk_fma_f32 v[40:41], v[42:43], s[16:17], v[138:139] op_sel_hi:[1,0,1]
	v_pk_fma_f32 v[36:37], v[36:37], s[16:17], v[132:133] op_sel_hi:[1,0,1]
	v_pk_mul_f32 v[40:41], v[40:41], v[50:51] op_sel_hi:[1,0]
	v_pk_fma_f32 v[32:33], v[32:33], s[16:17], v[128:129] op_sel_hi:[1,0,1]
	v_cvt_pk_fp8_f32 v166, v44, v45
	v_cvt_pk_fp8_f32 v167, v40, v41 op_sel:[0,0,1]
	v_pk_mul_f32 v[36:37], v[36:37], v[50:51] op_sel_hi:[1,0]
	v_pk_mul_f32 v[32:33], v[32:33], v[50:51] op_sel_hi:[1,0]
	v_mov_b32_e32 v168, 0
	v_mov_b32_e32 v169, 0
	v_cvt_pk_fp8_f32 v168, v36, v37
	v_cvt_pk_fp8_f32 v169, v32, v33
	v_pk_fma_f32 v[46:47], v[46:47], s[16:17], v[142:143] op_sel_hi:[1,0,1]
	v_pk_fma_f32 v[38:39], v[38:39], s[16:17], v[134:135] op_sel_hi:[1,0,1]
	v_pk_mul_f32 v[46:47], v[46:47], v[50:51] op_sel_hi:[1,0]
	v_pk_fma_f32 v[32:33], v[34:35], s[16:17], v[130:131] op_sel_hi:[1,0,1]
	v_ashrrev_i32_e32 v49, 31, v48
	v_cvt_pk_fp8_f32 v166, v46, v47 op_sel:[0,0,1]
	v_pk_mul_f32 v[38:39], v[38:39], v[50:51] op_sel_hi:[1,0]
	v_pk_mul_f32 v[32:33], v[32:33], v[50:51] op_sel_hi:[1,0]
	v_lshlrev_b64 v[48:49], 11, v[48:49]
	v_cvt_pk_fp8_f32 v168, v38, v39 op_sel:[0,0,1]
	v_cvt_pk_fp8_f32 v169, v32, v33 op_sel:[0,0,1]
	v_lshl_add_u64 v[32:33], s[12:13], 0, v[48:49]
	v_lshl_add_u64 v[32:33], v[32:33], 0, v[144:145]
	global_store_dwordx4 v[32:33], v[166:169], off
; DI unsigned pk4f8(float a, float b, float c, float d) { int p = __builtin_amdgcn_cvt_pk_fp8_f32(a, b, 0, false); p = __builtin_amdgcn_cvt_pk_fp8_f32(c, d, p, true); return (unsigned)p; }
;     __device__ __forceinline__ void operator()(const f32x4 (&acc)[2][2][4][2], const Unit& u, int wr, int wc, int fr, int fq) const {
;     ...
;             for (int m = 0; m < 4; ++m) { const int r = row0 + ai * HALF + m * 16;
;                 if (r < valid) { const int slot = slots[r]; const float w = wts[r]; unsigned char* rowp = ys + (size_t)slot * D + col0;
; #pragma unroll
;                     for (int bj = 0; bj < 2; ++bj) { const f32x4 v0 = (acc[ai][bj][m][0] * WSCALE_INV + bv[bj][0]) * w, v1 = (acc[ai][bj][m][1] * WSCALE_INV + bv[bj][1]) * w;
;                         u32x2 o; o.x = pk4f8(v0[0], v0[1], v0[2], v0[3]); o.y = pk4f8(v1[0], v1[1], v1[2], v1[3]);
;                         *(u32x2*)(rowp + bj * HALF) = o; } } }
.LBB0_1350:
	s_or_b64 exec, exec, s[2:3]
	v_add_u32_e32 v32, 0xa0, v160
	v_cmp_gt_i32_e32 vcc, s30, v32
	s_and_saveexec_b64 s[2:3], vcc
	s_cbranch_execz .LBB0_1352
	ds_read_b32 v32, v159 offset:640
	ds_read_b32 v34, v158 offset:640
	v_pk_fma_f32 v[24:25], v[24:25], s[16:17], v[136:137] op_sel_hi:[1,0,1]
	v_mov_b32_e32 v167, 0
	v_pk_fma_f32 v[28:29], v[28:29], s[16:17], v[140:141] op_sel_hi:[1,0,1]
	v_mov_b32_e32 v166, 0
	s_waitcnt lgkmcnt(0)
	v_pk_mul_f32 v[24:25], v[24:25], v[34:35] op_sel_hi:[1,0]
	v_pk_mul_f32 v[28:29], v[28:29], v[34:35] op_sel_hi:[1,0]
	v_cvt_pk_fp8_f32 v167, v24, v25
	v_pk_fma_f32 v[24:25], v[26:27], s[16:17], v[138:139] op_sel_hi:[1,0,1]
	v_pk_fma_f32 v[20:21], v[20:21], s[16:17], v[132:133] op_sel_hi:[1,0,1]
	v_pk_mul_f32 v[24:25], v[24:25], v[34:35] op_sel_hi:[1,0]
	v_pk_fma_f32 v[16:17], v[16:17], s[16:17], v[128:129] op_sel_hi:[1,0,1]
	v_cvt_pk_fp8_f32 v166, v28, v29
	v_cvt_pk_fp8_f32 v167, v24, v25 op_sel:[0,0,1]
	v_pk_mul_f32 v[20:21], v[20:21], v[34:35] op_sel_hi:[1,0]
	v_pk_mul_f32 v[16:17], v[16:17], v[34:35] op_sel_hi:[1,0]
	v_mov_b32_e32 v168, 0
	v_mov_b32_e32 v169, 0
	v_cvt_pk_fp8_f32 v168, v20, v21
	v_cvt_pk_fp8_f32 v169, v16, v17
	v_pk_fma_f32 v[30:31], v[30:31], s[16:17], v[142:143] op_sel_hi:[1,0,1]
	v_pk_fma_f32 v[22:23], v[22:23], s[16:17], v[134:135] op_sel_hi:[1,0,1]
	v_pk_mul_f32 v[30:31], v[30:31], v[34:35] op_sel_hi:[1,0]
	v_pk_fma_f32 v[16:17], v[18:19], s[16:17], v[130:131] op_sel_hi:[1,0,1]
	v_ashrrev_i32_e32 v33, 31, v32
	v_cvt_pk_fp8_f32 v166, v30, v31 op_sel:[0,0,1]
	v_pk_mul_f32 v[22:23], v[22:23], v[34:35] op_sel_hi:[1,0]
	v_pk_mul_f32 v[16:17], v[16:17], v[34:35] op_sel_hi:[1,0]
	v_lshlrev_b64 v[32:33], 11, v[32:33]
	v_cvt_pk_fp8_f32 v168, v22, v23 op_sel:[0,0,1]
	v_cvt_pk_fp8_f32 v169, v16, v17 op_sel:[0,0,1]
	v_lshl_add_u64 v[16:17], s[12:13], 0, v[32:33]
	v_lshl_add_u64 v[16:17], v[16:17], 0, v[144:145]
	global_store_dwordx4 v[16:17], v[166:169], off
.LBB0_1352:
	s_or_b64 exec, exec, s[2:3]
	v_add_u32_e32 v16, 0xb0, v160
	v_cmp_gt_i32_e32 vcc, s30, v16
	s_and_saveexec_b64 s[2:3], vcc
	s_cbranch_execz .LBB0_1354
	ds_read_b32 v16, v159 offset:704
	ds_read_b32 v18, v158 offset:704
	v_pk_fma_f32 v[8:9], v[8:9], s[16:17], v[136:137] op_sel_hi:[1,0,1]
	v_mov_b32_e32 v167, 0
	v_pk_fma_f32 v[12:13], v[12:13], s[16:17], v[140:141] op_sel_hi:[1,0,1]
	v_mov_b32_e32 v166, 0
	s_waitcnt lgkmcnt(0)
	v_pk_mul_f32 v[8:9], v[8:9], v[18:19] op_sel_hi:[1,0]
	v_pk_mul_f32 v[12:13], v[12:13], v[18:19] op_sel_hi:[1,0]
	v_cvt_pk_fp8_f32 v167, v8, v9
	v_pk_fma_f32 v[8:9], v[10:11], s[16:17], v[138:139] op_sel_hi:[1,0,1]
	v_pk_fma_f32 v[4:5], v[4:5], s[16:17], v[132:133] op_sel_hi:[1,0,1]
	v_pk_mul_f32 v[8:9], v[8:9], v[18:19] op_sel_hi:[1,0]
	v_pk_fma_f32 v[0:1], v[0:1], s[16:17], v[128:129] op_sel_hi:[1,0,1]
	v_cvt_pk_fp8_f32 v166, v12, v13
	v_cvt_pk_fp8_f32 v167, v8, v9 op_sel:[0,0,1]
	v_pk_mul_f32 v[4:5], v[4:5], v[18:19] op_sel_hi:[1,0]
	v_pk_mul_f32 v[0:1], v[0:1], v[18:19] op_sel_hi:[1,0]
	v_mov_b32_e32 v168, 0
	v_mov_b32_e32 v169, 0
	v_cvt_pk_fp8_f32 v168, v4, v5
	v_cvt_pk_fp8_f32 v169, v0, v1
	v_pk_fma_f32 v[14:15], v[14:15], s[16:17], v[142:143] op_sel_hi:[1,0,1]
	v_pk_fma_f32 v[6:7], v[6:7], s[16:17], v[134:135] op_sel_hi:[1,0,1]
	v_pk_mul_f32 v[14:15], v[14:15], v[18:19] op_sel_hi:[1,0]
	v_pk_fma_f32 v[0:1], v[2:3], s[16:17], v[130:131] op_sel_hi:[1,0,1]
	v_ashrrev_i32_e32 v17, 31, v16
	v_cvt_pk_fp8_f32 v166, v14, v15 op_sel:[0,0,1]
	v_pk_mul_f32 v[6:7], v[6:7], v[18:19] op_sel_hi:[1,0]
	v_pk_mul_f32 v[0:1], v[0:1], v[18:19] op_sel_hi:[1,0]
	v_lshlrev_b64 v[16:17], 11, v[16:17]
	v_cvt_pk_fp8_f32 v168, v6, v7 op_sel:[0,0,1]
	v_cvt_pk_fp8_f32 v169, v0, v1 op_sel:[0,0,1]
	v_lshl_add_u64 v[0:1], s[12:13], 0, v[16:17]
	v_lshl_add_u64 v[0:1], v[0:1], 0, v[144:145]
	global_store_dwordx4 v[0:1], v[166:169], off
